# P2 attention units dealt XCD-locally (each XCD computes the token range whose P3 row tiles it owns); the P2->P3 barrier skips the L2 write-back unless the placement flag is raised
# speedup vs baseline: 1.0206x; 1.0031x over previous
.LBB0_639:
	s_or_b64 exec, exec, s[0:1]
	v_readfirstlane_b32 s6, v2
	s_cmp_ge_i32 s6, s79
	s_mov_b64 s[0:1], 0
	s_cbranch_scc1 .LBB0_435
	s_cmp_lt_i32 s6, s35
	v_readlane_b32 s0, v255, 58
	v_readlane_b32 s1, v255, 57
	s_cselect_b32 s68, s1, s0
	s_add_i32 s68, s68, s6
	v_readlane_b32 s0, v255, 2
	s_cmpk_lg_i32 s0, 0x100
	s_cbranch_scc1 .Lremap_done
	v_readlane_b32 s0, v255, 8
	s_lshr_b32 s1, s0, 5
	s_and_b32 s0, s0, 31
	s_lshr_b32 s8, s1, 2
	s_and_b32 s1, s1, 3
	s_lshr_b32 s10, s0, 3
	s_and_b32 s0, s0, 7
	s_cmp_lt_i32 s6, s35
	s_cbranch_scc0 .Lremap_a
	s_lshl_b32 s8, s8, 2
	s_or_b32 s8, s8, s10
	s_lshl_b32 s8, s8, 5
	s_lshl_b32 s1, s1, 3
	s_or_b32 s1, s1, s0
	s_or_b32 s8, s8, s1
	s_lshl_b32 s8, s8, 3
	s_or_b32 s8, s8, s6
	s_add_i32 s68, s8, 0x1000
	s_branch .Lremap_done
.Lremap_a:
	s_sub_i32 s68, s6, s35
	s_lshl_b32 s0, s0, 4
	s_add_i32 s68, s68, s0
	s_lshl_b32 s1, s1, 7
	s_add_i32 s68, s68, s1
	s_lshl_b32 s10, s10, 9
	s_or_b32 s68, s68, s10
	s_lshl_b32 s8, s8, 11
	s_or_b32 s68, s68, s8
.Lremap_done:
	s_cmp_ge_i32 s6, s35
	s_cbranch_scc0 .LBB0_744
	s_cmpk_lt_i32 s68, 0x1000
	s_cselect_b64 s[0:1], -1, 0
	s_cbranch_execz .LBB0_745
	s_branch .LBB0_746

.LBB0_836:
	s_mov_b64 s[16:17], exec
	v_mbcnt_lo_u32_b32 v3, s16, 0
	v_mbcnt_hi_u32_b32 v3, s17, v3
	v_cmp_eq_u32_e32 vcc, 0, v3
	s_and_saveexec_b64 s[6:7], vcc
	s_cbranch_execz .LBB0_838
	v_readlane_b32 s8, v255, 11
	s_lshl_b32 s8, s8, 8
	v_readlane_b32 s10, v255, 9
	v_readlane_b32 s11, v255, 10
	s_add_u32 s8, s10, s8
	s_addc_u32 s9, s11, 0
	v_mov_b32_e32 v200, 0x3000
	s_nop 2
	global_load_dword v200, v200, s[10:11] offset:896 sc1
	s_bcnt1_i32_b64 s10, s[16:17]
	v_mov_b32_e32 v5, 0x1000
	v_mov_b32_e32 v6, s10
	global_atomic_add v5, v5, v6, s[8:9] offset:1024 sc0
	buffer_inv sc1

.LBB0_852:
	s_andn2_saveexec_b64 s[6:7], s[6:7]
	s_cbranch_execz .LBB0_870
	v_cmp_eq_u32_e32 vcc, 0, v200
	s_cbranch_vccnz .Lskip_wb2
	buffer_wbl2 sc1
.Lskip_wb2:
	v_readlane_b32 s16, v255, 9
	v_readlane_b32 s17, v255, 10
	v_mov_b32_e32 v6, 0x20164
	ds_read_b32 v6, v6
	s_waitcnt vmcnt(0) lgkmcnt(0)
	v_add_u32_e32 v3, 1, v3
	v_mul_lo_u32 v3, v3, v6
	v_mov_b32_e32 v6, 0x3000
	v_mov_b32_e32 v5, 1
	s_mov_b32 s8, 0
	global_atomic_add v6, v5, s[16:17] offset:1024
